# L2: software-pipelined task fetch (next task id, rowptr, CSR indices, batch_vec prefetched); bucketsort LDS reads hoisted
# baseline (speedup 1.0000x reference)
.LBB5_11:
	s_or_b64 exec, exec, s[6:7]
	s_cmp_eq_u32 s41, 0
	s_cbranch_scc1 .LBB5_118
	s_mov_b32 s33, s42
	v_mov_b32_e32 v4, v102
	v_mov_b32_e32 v5, v103
	v_mov_b32_e32 v6, v104
	v_mov_b32_e32 v7, v105
	s_branch .Lp2_have_cur
.LBB5_13:
	v_mov_b32_e32 v0, 0
	s_and_saveexec_b64 s[6:7], s[0:1]
	v_mov_b32_e32 v1, 1
	ds_add_rtn_u32 v0, v33, v1 offset:52224
	s_mov_b64 exec, s[6:7]
	s_waitcnt lgkmcnt(0)
	v_readfirstlane_b32 s8, v0
	s_cmp_ge_i32 s8, s21
	s_cbranch_scc1 .LBB5_118
	s_lshl_b32 s33, s8, 3
	s_add_i32 s33, s33, s20
	v_add_u32_e32 v8, s33, v74
	v_cmp_gt_i32_e32 vcc, s28, v8
	v_mov_b32_e32 v4, 0
	v_mov_b32_e32 v5, 0
	v_mov_b32_e32 v6, 0
	v_mov_b32_e32 v7, 0
	s_and_saveexec_b64 s[6:7], vcc
	v_lshl_add_u32 v2, v8, 1, v8
	v_lshlrev_b32_e32 v2, 2, v2
	global_load_dwordx4 v[4:7], v2, s[14:15]
	s_mov_b64 exec, s[6:7]
	s_waitcnt vmcnt(0)
	v_mov_b32_e32 v106, 0x186a0
	v_mov_b32_e32 v107, 0x186a0
	v_mov_b32_e32 v108, 0x186a0
	v_mov_b32_e32 v109, 0x186a0
	v_mov_b32_e32 v110, 0x186a0
	v_mov_b32_e32 v111, 0x186a0
	v_mov_b32_e32 v112, 0x186a0
	v_mov_b32_e32 v113, 0x186a0
	v_mov_b32_e32 v114, 0x186a0
	s_mov_b64 s[6:7], exec
	v_add_u32_e32 v116, v4, v75
	v_lshlrev_b32_e32 v117, 2, v116
	v_cmp_lt_i32_e32 vcc, v116, v5
	s_and_b64 exec, exec, vcc
	global_load_dword v106, v117, s[26:27]
	v_add_u32_e32 v116, 8, v116
	v_cmp_lt_i32_e32 vcc, v116, v5
	s_and_b64 exec, exec, vcc
	global_load_dword v107, v117, s[26:27] offset:32
	v_add_u32_e32 v116, 8, v116
	v_cmp_lt_i32_e32 vcc, v116, v5
	s_and_b64 exec, exec, vcc
	global_load_dword v108, v117, s[26:27] offset:64
	s_mov_b64 exec, s[6:7]
	v_add_u32_e32 v116, v5, v75
	v_lshlrev_b32_e32 v117, 2, v116
	v_cmp_lt_i32_e32 vcc, v116, v6
	s_and_b64 exec, exec, vcc
	global_load_dword v109, v117, s[26:27]
	v_add_u32_e32 v116, 8, v116
	v_cmp_lt_i32_e32 vcc, v116, v6
	s_and_b64 exec, exec, vcc
	global_load_dword v110, v117, s[26:27] offset:32
	v_add_u32_e32 v116, 8, v116
	v_cmp_lt_i32_e32 vcc, v116, v6
	s_and_b64 exec, exec, vcc
	global_load_dword v111, v117, s[26:27] offset:64
	s_mov_b64 exec, s[6:7]
	v_add_u32_e32 v116, v6, v75
	v_lshlrev_b32_e32 v117, 2, v116
	v_cmp_lt_i32_e32 vcc, v116, v7
	s_and_b64 exec, exec, vcc
	global_load_dword v112, v117, s[26:27]
	v_add_u32_e32 v116, 8, v116
	v_cmp_lt_i32_e32 vcc, v116, v7
	s_and_b64 exec, exec, vcc
	global_load_dword v113, v117, s[26:27] offset:32
	v_add_u32_e32 v116, 8, v116
	v_cmp_lt_i32_e32 vcc, v116, v7
	s_and_b64 exec, exec, vcc
	global_load_dword v114, v117, s[26:27] offset:64
	s_mov_b64 exec, s[6:7]
	s_waitcnt vmcnt(0)
.Lp2_have_cur:
	s_and_saveexec_b64 s[6:7], s[0:1]
	v_mov_b32_e32 v11, 1
	ds_add_rtn_u32 v10, v33, v11 offset:52224
	s_mov_b64 exec, s[6:7]
	v_sub_u32_e32 v58, v5, v4
	v_sub_u32_e32 v87, v6, v5
	v_sub_u32_e32 v85, v7, v6
	v_lshlrev_b32_e32 v9, 6, v106
	v_lshlrev_b32_e32 v8, 6, v107
	v_lshlrev_b32_e32 v60, 6, v108
	v_lshlrev_b32_e32 v59, 6, v109
	v_lshlrev_b32_e32 v62, 6, v110
	v_lshlrev_b32_e32 v89, 6, v111
	v_lshlrev_b32_e32 v88, 6, v112
	v_lshlrev_b32_e32 v86, 6, v113
	v_lshlrev_b32_e32 v7, 6, v114
	v_and_b32_e32 v9, 0x7fffc0, v9
	v_and_b32_e32 v8, 0x7fffc0, v8
	v_and_b32_e32 v60, 0x7fffc0, v60
	v_and_b32_e32 v59, 0x7fffc0, v59
	v_and_b32_e32 v62, 0x7fffc0, v62
	v_and_b32_e32 v89, 0x7fffc0, v89
	v_and_b32_e32 v88, 0x7fffc0, v88
	v_and_b32_e32 v86, 0x7fffc0, v86
	v_and_b32_e32 v7, 0x7fffc0, v7
	v_add_u32_e32 v12, s33, v74
	v_mov_b32_e32 v0, 0
	v_mov_b32_e32 v1, 0
	v_mov_b32_e32 v2, 0
	v_mov_b32_e32 v3, 0
	v_mov_b32_e32 v115, -1
	v_cmp_gt_i32_e32 vcc, s28, v12
	s_and_saveexec_b64 s[6:7], vcc
	v_lshl_or_b32 v12, v12, 7, v76
	global_load_dwordx4 v[0:3], v12, s[12:13]
	s_mov_b64 exec, s[6:7]
	v_add_u32_e32 v13, s33, v77
	v_cmp_gt_i32_e32 vcc, s28, v13
	s_and_b64 s[8:9], s[2:3], vcc
	s_and_saveexec_b64 s[6:7], s[8:9]
	v_lshlrev_b32_e32 v13, 2, v13
	global_load_dword v115, v13, s[16:17]
	s_mov_b64 exec, s[6:7]
	v_mov_b32_e32 v102, 0
	v_mov_b32_e32 v103, 0
	v_mov_b32_e32 v104, 0
	v_mov_b32_e32 v105, 0
	s_waitcnt lgkmcnt(0)
	v_readfirstlane_b32 s40, v10
	s_cmp_lt_i32 s40, s21
	s_cselect_b32 s41, 1, 0
	s_cbranch_scc0 .Lp2_no_next
	s_lshl_b32 s42, s40, 3
	s_add_i32 s42, s42, s20
	v_add_u32_e32 v14, s42, v74
	v_cmp_gt_i32_e32 vcc, s28, v14
	s_and_saveexec_b64 s[6:7], vcc
	v_lshl_add_u32 v14, v14, 1, v14
	v_lshlrev_b32_e32 v14, 2, v14
	global_load_dwordx4 v[102:105], v14, s[14:15]
	s_mov_b64 exec, s[6:7]
.Lp2_no_next:
	ds_swizzle_b32 v10, v9 offset:swizzle(BROADCAST,8,0)
	ds_swizzle_b32 v11, v9 offset:swizzle(BROADCAST,8,1)
	ds_swizzle_b32 v13, v9 offset:swizzle(BROADCAST,8,3)
	ds_swizzle_b32 v12, v9 offset:swizzle(BROADCAST,8,2)
	ds_swizzle_b32 v14, v9 offset:swizzle(BROADCAST,8,4)
	ds_swizzle_b32 v15, v9 offset:swizzle(BROADCAST,8,5)
	s_waitcnt lgkmcnt(0)
	v_add_u32_e32 v10, v10, v81
	v_add_u32_e32 v11, v11, v81
	v_add_u32_e32 v13, v13, v81
	ds_swizzle_b32 v16, v9 offset:swizzle(BROADCAST,8,6)
	ds_swizzle_b32 v9, v9 offset:swizzle(BROADCAST,8,7)
	v_add_u32_e32 v12, v12, v81
	global_load_dwordx2 v[56:57], v10, s[30:31]
	global_load_dwordx2 v[52:53], v11, s[30:31]
	global_load_dwordx2 v[30:31], v12, s[30:31]
	global_load_dwordx2 v[24:25], v13, s[30:31]
	v_add_u32_e32 v10, v14, v81
	v_add_u32_e32 v11, v15, v81
	ds_swizzle_b32 v13, v8 offset:swizzle(BROADCAST,8,0)
	ds_swizzle_b32 v14, v8 offset:swizzle(BROADCAST,8,1)
	ds_swizzle_b32 v15, v8 offset:swizzle(BROADCAST,8,2)
	s_waitcnt lgkmcnt(3)
	v_add_u32_e32 v9, v9, v81
	v_add_u32_e32 v12, v16, v81
	ds_swizzle_b32 v16, v8 offset:swizzle(BROADCAST,8,3)
	global_load_dwordx2 v[54:55], v10, s[30:31]
	global_load_dwordx2 v[50:51], v11, s[30:31]
	global_load_dwordx2 v[26:27], v12, s[30:31]
	global_load_dwordx2 v[20:21], v9, s[30:31]
	s_waitcnt lgkmcnt(3)
	v_add_u32_e32 v9, v13, v81
	s_waitcnt lgkmcnt(2)
	v_add_u32_e32 v10, v14, v81
	s_waitcnt lgkmcnt(1)
	v_add_u32_e32 v11, v15, v81
	ds_swizzle_b32 v13, v8 offset:swizzle(BROADCAST,8,4)
	ds_swizzle_b32 v14, v8 offset:swizzle(BROADCAST,8,5)
	ds_swizzle_b32 v15, v8 offset:swizzle(BROADCAST,8,6)
	ds_swizzle_b32 v8, v8 offset:swizzle(BROADCAST,8,7)
	s_waitcnt lgkmcnt(4)
	v_add_u32_e32 v12, v16, v81
	global_load_dwordx2 v[28:29], v9, s[30:31]
	global_load_dwordx2 v[22:23], v10, s[30:31]
	global_load_dwordx2 v[18:19], v11, s[30:31]
	global_load_dwordx2 v[16:17], v12, s[30:31]
	s_waitcnt lgkmcnt(3)
	v_add_u32_e32 v9, v13, v81
	s_waitcnt lgkmcnt(2)
	v_add_u32_e32 v10, v14, v81
	s_waitcnt lgkmcnt(1)
	v_add_u32_e32 v11, v15, v81
	s_waitcnt lgkmcnt(0)
	v_add_u32_e32 v8, v8, v81
	global_load_dwordx2 v[14:15], v9, s[30:31]
	global_load_dwordx2 v[12:13], v10, s[30:31]
	s_nop 0
	global_load_dwordx2 v[10:11], v11, s[30:31]
	s_nop 0
	global_load_dwordx2 v[8:9], v8, s[30:31]
	v_cmp_lt_i32_e32 vcc, 16, v58
	s_cmp_lg_u64 vcc, 0
	s_cselect_b64 s[36:37], -1, 0
	v_cmp_lt_i32_e64 s[10:11], 18, v58
	v_cmp_lt_i32_e64 s[8:9], 20, v58
	v_cmp_lt_i32_e64 s[6:7], 22, v58
	s_cbranch_vccz .LBB5_42
	ds_swizzle_b32 v34, v60 offset:swizzle(BROADCAST,8,0)
	ds_swizzle_b32 v35, v60 offset:swizzle(BROADCAST,8,1)
	s_waitcnt lgkmcnt(1)
	v_add_u32_e32 v34, v34, v81
	s_waitcnt lgkmcnt(0)
	v_add_u32_e32 v38, v35, v81
	global_load_dwordx2 v[34:35], v34, s[30:31]
	s_nop 0
	global_load_dwordx2 v[38:39], v38, s[30:31]

.LBB5_61:
	s_cbranch_execz .LBB5_58
	v_mov_b32_e32 v106, 0x186a0
	v_mov_b32_e32 v107, 0x186a0
	v_mov_b32_e32 v108, 0x186a0
	v_mov_b32_e32 v109, 0x186a0
	v_mov_b32_e32 v110, 0x186a0
	v_mov_b32_e32 v111, 0x186a0
	v_mov_b32_e32 v112, 0x186a0
	v_mov_b32_e32 v113, 0x186a0
	v_mov_b32_e32 v114, 0x186a0
	s_mov_b64 s[6:7], exec
	v_add_u32_e32 v116, v102, v75
	v_lshlrev_b32_e32 v117, 2, v116
	v_cmp_lt_i32_e32 vcc, v116, v103
	s_and_b64 exec, exec, vcc
	global_load_dword v106, v117, s[26:27]
	v_add_u32_e32 v116, 8, v116
	v_cmp_lt_i32_e32 vcc, v116, v103
	s_and_b64 exec, exec, vcc
	global_load_dword v107, v117, s[26:27] offset:32
	v_add_u32_e32 v116, 8, v116
	v_cmp_lt_i32_e32 vcc, v116, v103
	s_and_b64 exec, exec, vcc
	global_load_dword v108, v117, s[26:27] offset:64
	s_mov_b64 exec, s[6:7]
	v_add_u32_e32 v116, v103, v75
	v_lshlrev_b32_e32 v117, 2, v116
	v_cmp_lt_i32_e32 vcc, v116, v104
	s_and_b64 exec, exec, vcc
	global_load_dword v109, v117, s[26:27]
	v_add_u32_e32 v116, 8, v116
	v_cmp_lt_i32_e32 vcc, v116, v104
	s_and_b64 exec, exec, vcc
	global_load_dword v110, v117, s[26:27] offset:32
	v_add_u32_e32 v116, 8, v116
	v_cmp_lt_i32_e32 vcc, v116, v104
	s_and_b64 exec, exec, vcc
	global_load_dword v111, v117, s[26:27] offset:64
	s_mov_b64 exec, s[6:7]
	v_add_u32_e32 v116, v104, v75
	v_lshlrev_b32_e32 v117, 2, v116
	v_cmp_lt_i32_e32 vcc, v116, v105
	s_and_b64 exec, exec, vcc
	global_load_dword v112, v117, s[26:27]
	v_add_u32_e32 v116, 8, v116
	v_cmp_lt_i32_e32 vcc, v116, v105
	s_and_b64 exec, exec, vcc
	global_load_dword v113, v117, s[26:27] offset:32
	v_add_u32_e32 v116, 8, v116
	v_cmp_lt_i32_e32 vcc, v116, v105
	s_and_b64 exec, exec, vcc
	global_load_dword v114, v117, s[26:27] offset:64
	s_mov_b64 exec, s[6:7]
	ds_write_b128 v82, v[8:11] offset:33792
	ds_read_b128 v[8:11], v83
	ds_read_b128 v[12:15], v80 offset:33792
	ds_read_b128 v[16:19], v83 offset:8448
	ds_read_b128 v[20:23], v83 offset:16896
	ds_read_b128 v[24:27], v83 offset:25344
	s_waitcnt lgkmcnt(3)
	v_mfma_f32_16x16x32_f16 v[8:11], v[8:11], v[12:15], 0
	s_waitcnt lgkmcnt(2)
	v_mfma_f32_16x16x32_f16 v[16:19], v[16:19], v[12:15], 0
	s_waitcnt lgkmcnt(1)
	v_mfma_f32_16x16x32_f16 v[20:23], v[20:23], v[12:15], 0
	s_waitcnt lgkmcnt(0)
	v_mfma_f32_16x16x32_f16 v[90:93], v[24:27], v[12:15], 0
	ds_read_b128 v[12:15], v83 offset:64
	ds_read_b128 v[94:97], v80 offset:33856
	ds_read_b128 v[24:27], v83 offset:8512
	ds_read_b128 v[98:101], v83 offset:16960
	ds_swizzle_b32 v4, v59 offset:swizzle(BROADCAST,8,0)
	ds_swizzle_b32 v28, v59 offset:swizzle(BROADCAST,8,1)
	s_waitcnt lgkmcnt(4)
	v_mfma_f32_16x16x32_f16 v[8:11], v[12:15], v[94:97], v[8:11]
	ds_swizzle_b32 v29, v59 offset:swizzle(BROADCAST,8,2)
	ds_swizzle_b32 v30, v59 offset:swizzle(BROADCAST,8,3)
	s_waitcnt lgkmcnt(3)
	v_add_u32_e32 v4, v4, v81
	v_mfma_f32_16x16x32_f16 v[12:15], v[24:27], v[94:97], v[16:19]
	ds_swizzle_b32 v24, v59 offset:swizzle(BROADCAST,8,5)
	ds_swizzle_b32 v25, v59 offset:swizzle(BROADCAST,8,6)
	ds_swizzle_b32 v26, v59 offset:swizzle(BROADCAST,8,7)
	ds_swizzle_b32 v19, v59 offset:swizzle(BROADCAST,8,4)
	s_waitcnt lgkmcnt(6)
	v_add_u32_e32 v16, v28, v81
	s_waitcnt lgkmcnt(5)
	v_add_u32_e32 v17, v29, v81
	s_waitcnt lgkmcnt(4)
	v_add_u32_e32 v18, v30, v81
	global_load_dwordx2 v[72:73], v4, s[30:31]
	global_load_dwordx2 v[68:69], v16, s[30:31]
	global_load_dwordx2 v[64:65], v17, s[30:31]
	global_load_dwordx2 v[58:59], v18, s[30:31]
	s_waitcnt lgkmcnt(0)
	v_add_u32_e32 v4, v19, v81
	ds_swizzle_b32 v19, v62 offset:swizzle(BROADCAST,8,0)
	v_add_u32_e32 v16, v24, v81
	v_add_u32_e32 v17, v25, v81
	v_add_u32_e32 v18, v26, v81
	ds_swizzle_b32 v24, v62 offset:swizzle(BROADCAST,8,1)
	ds_swizzle_b32 v25, v62 offset:swizzle(BROADCAST,8,2)
	ds_swizzle_b32 v26, v62 offset:swizzle(BROADCAST,8,3)
	global_load_dwordx2 v[70:71], v4, s[30:31]
	global_load_dwordx2 v[66:67], v16, s[30:31]
	global_load_dwordx2 v[60:61], v17, s[30:31]
	global_load_dwordx2 v[54:55], v18, s[30:31]
	s_waitcnt lgkmcnt(3)
	v_add_u32_e32 v4, v19, v81
	ds_swizzle_b32 v19, v62 offset:swizzle(BROADCAST,8,4)
	s_waitcnt lgkmcnt(3)
	v_add_u32_e32 v16, v24, v81
	s_waitcnt lgkmcnt(2)
	v_add_u32_e32 v17, v25, v81
	s_waitcnt lgkmcnt(1)
	v_add_u32_e32 v18, v26, v81
	ds_swizzle_b32 v24, v62 offset:swizzle(BROADCAST,8,5)
	ds_swizzle_b32 v25, v62 offset:swizzle(BROADCAST,8,6)
	ds_swizzle_b32 v26, v62 offset:swizzle(BROADCAST,8,7)
	global_load_dwordx2 v[62:63], v4, s[30:31]
	global_load_dwordx2 v[56:57], v16, s[30:31]
	global_load_dwordx2 v[52:53], v17, s[30:31]
	global_load_dwordx2 v[50:51], v18, s[30:31]
	s_waitcnt lgkmcnt(3)
	v_add_u32_e32 v4, v19, v81
	s_waitcnt lgkmcnt(2)
	v_add_u32_e32 v16, v24, v81
	s_waitcnt lgkmcnt(1)
	v_add_u32_e32 v17, v25, v81
	s_waitcnt lgkmcnt(0)
	v_add_u32_e32 v18, v26, v81
	global_load_dwordx2 v[30:31], v4, s[30:31]
	global_load_dwordx2 v[28:29], v16, s[30:31]
	global_load_dwordx2 v[26:27], v17, s[30:31]
	global_load_dwordx2 v[24:25], v18, s[30:31]
	v_mfma_f32_16x16x32_f16 v[16:19], v[98:101], v[94:97], v[20:23]
	v_cmp_lt_i32_e32 vcc, 16, v87
	s_cmp_lg_u64 vcc, 0
	s_cselect_b64 s[36:37], -1, 0
	ds_read_b128 v[20:23], v83 offset:25408
	s_waitcnt lgkmcnt(0)
	v_mfma_f32_16x16x32_f16 v[20:23], v[20:23], v[94:97], v[90:93]
	v_cmp_lt_i32_e64 s[10:11], 18, v87
	v_cmp_lt_i32_e64 s[8:9], 20, v87
	v_cmp_lt_i32_e64 s[6:7], 22, v87
	s_cbranch_vccz .LBB5_64
	ds_swizzle_b32 v4, v89 offset:swizzle(BROADCAST,8,0)
	ds_swizzle_b32 v34, v89 offset:swizzle(BROADCAST,8,1)
	s_waitcnt lgkmcnt(1)
	v_add_u32_e32 v4, v4, v81
	s_waitcnt lgkmcnt(0)
	v_add_u32_e32 v38, v34, v81
	global_load_dwordx2 v[34:35], v4, s[30:31]
	s_nop 0
	global_load_dwordx2 v[38:39], v38, s[30:31]

.LBB5_105:
	s_cbranch_execz .LBB5_102
	ds_write_b128 v82, v[4:7] offset:33792
	ds_read_b128 v[4:7], v83 offset:256
	ds_read_b128 v[24:27], v80 offset:33792
	ds_read_b128 v[28:31], v83 offset:8704
	s_waitcnt lgkmcnt(1)
	v_mfma_f32_16x16x32_f16 v[4:7], v[4:7], v[24:27], v[8:11]
	s_nop 2
	ds_read_b128 v[8:11], v83 offset:17152
	s_waitcnt lgkmcnt(1)
	v_mfma_f32_16x16x32_f16 v[12:15], v[28:31], v[24:27], v[12:15]
	s_waitcnt lgkmcnt(0)
	v_mfma_f32_16x16x32_f16 v[8:11], v[8:11], v[24:27], v[16:19]
	s_nop 2
	ds_read_b128 v[16:19], v83 offset:25600
	s_waitcnt lgkmcnt(0)
	v_mfma_f32_16x16x32_f16 v[16:19], v[16:19], v[24:27], v[20:23]
	s_nop 2
	ds_read_b128 v[20:23], v83 offset:320
	ds_read_b128 v[24:27], v80 offset:33856
	ds_read_b128 v[28:31], v83 offset:8768
	s_waitcnt lgkmcnt(1)
	v_mfma_f32_16x16x32_f16 v[4:7], v[20:23], v[24:27], v[4:7]
	ds_read_b128 v[20:23], v83 offset:17216
	s_waitcnt lgkmcnt(1)
	v_mfma_f32_16x16x32_f16 v[12:15], v[28:31], v[24:27], v[12:15]
	s_waitcnt lgkmcnt(0)
	v_mfma_f32_16x16x32_f16 v[8:11], v[20:23], v[24:27], v[8:11]
	ds_read_b128 v[20:23], v83 offset:25664
	ds_write_b128 v82, v[0:3] offset:33792
	s_waitcnt lgkmcnt(1)
	v_mfma_f32_16x16x32_f16 v[0:3], v[20:23], v[24:27], v[16:19]
	s_nop 2
	ds_read_b128 v[16:19], v83 offset:384
	ds_read_b128 v[20:23], v80 offset:33792
	ds_read_b128 v[24:27], v83 offset:8832
	s_waitcnt lgkmcnt(1)
	v_mfma_f32_16x16x32_f16 v[4:7], v[16:19], v[20:23], v[4:7]
	ds_read_b128 v[16:19], v83 offset:17280
	s_waitcnt lgkmcnt(1)
	v_mfma_f32_16x16x32_f16 v[12:15], v[24:27], v[20:23], v[12:15]
	s_waitcnt lgkmcnt(0)
	v_mfma_f32_16x16x32_f16 v[8:11], v[16:19], v[20:23], v[8:11]
	ds_read_b128 v[16:19], v83 offset:25728
	s_waitcnt lgkmcnt(0)
	v_mfma_f32_16x16x32_f16 v[0:3], v[16:19], v[20:23], v[0:3]
	ds_read_b128 v[16:19], v83 offset:448
	ds_read_b128 v[20:23], v80 offset:33856
	ds_read_b128 v[24:27], v83 offset:8896
	ds_read_b128 v[28:31], v83 offset:17344
	ds_read_b128 v[50:53], v83 offset:25792
	s_mov_b64 s[6:7], s[22:23]
	s_mov_b64 s[8:9], s[18:19]
	s_waitcnt lgkmcnt(1)
	v_mfma_f32_16x16x32_f16 v[8:11], v[28:31], v[20:23], v[8:11]
	s_nop 0
	s_waitcnt lgkmcnt(0)
	v_mfma_f32_16x16x32_f16 v[0:3], v[50:53], v[20:23], v[0:3]
	v_mfma_f32_16x16x32_f16 v[16:19], v[16:19], v[20:23], v[4:7]
	s_nop 2
	v_add_u32_e32 v6, s33, v77
	v_mfma_f32_16x16x32_f16 v[12:15], v[24:27], v[20:23], v[12:15]
	v_cmp_gt_i32_e32 vcc, s28, v6
	ds_read_b128 v[20:23], v32 offset:52240
	ds_read_b128 v[24:27], v32 offset:52496
	ds_read_b128 v[28:31], v32 offset:52752
	s_waitcnt lgkmcnt(0)
	v_add_f32_e32 v7, v16, v20
	v_mov_b32_e32 v4, v24
	v_mov_b32_e32 v5, v28
	v_add_f32_e32 v16, v17, v21
	v_add_f32_e32 v17, v18, v22
	v_add_f32_e32 v18, v19, v23
	v_max_f32_e32 v24, 0, v7
	v_max_f32_e32 v62, 0, v16
	v_max_f32_e32 v64, 0, v17
	v_max_f32_e32 v66, 0, v18
	ds_read_b128 v[16:19], v32 offset:52304
	ds_read_b128 v[20:23], v32 offset:52560
	ds_read_b128 v[50:53], v32 offset:52816
	s_waitcnt lgkmcnt(0)
	v_add_f32_e32 v7, v12, v16
	v_add_f32_e32 v12, v13, v17
	v_add_f32_e32 v13, v14, v18
	v_add_f32_e32 v14, v15, v19
	v_max_f32_e32 v68, 0, v7
	v_max_f32_e32 v70, 0, v12
	v_max_f32_e32 v72, 0, v13
	v_max_f32_e32 v86, 0, v14
	ds_read_b128 v[12:15], v32 offset:52368
	ds_read_b128 v[16:19], v32 offset:52624
	ds_read_b128 v[54:57], v32 offset:52880
	v_pk_fma_f32 v[88:89], v[4:5], v[24:25], 0 op_sel_hi:[1,0,0]
	v_mov_b32_e32 v28, v25
	v_mov_b32_e32 v24, v26
	v_mov_b32_e32 v25, v30
	v_mov_b32_e32 v30, v27
	v_mov_b32_e32 v26, v20
	v_mov_b32_e32 v27, v50
	v_mov_b32_e32 v50, v21
	v_mov_b32_e32 v20, v22
	v_mov_b32_e32 v21, v52
	v_mov_b32_e32 v52, v23
	v_pk_fma_f32 v[22:23], v[28:29], v[62:63], v[88:89] op_sel_hi:[1,0,1]
	v_mov_b32_e32 v4, v33
	v_pk_fma_f32 v[22:23], v[24:25], v[64:65], v[22:23] op_sel_hi:[1,0,1]
	v_mov_b32_e32 v5, v33
	v_pk_fma_f32 v[22:23], v[30:31], v[66:67], v[22:23] op_sel_hi:[1,0,1]
	s_waitcnt lgkmcnt(0)
	v_add_f32_e32 v7, v8, v12
	v_pk_fma_f32 v[22:23], v[26:27], v[68:69], v[22:23] op_sel_hi:[1,0,1]
	v_mov_b32_e32 v8, v16
	v_pk_fma_f32 v[22:23], v[50:51], v[70:71], v[22:23] op_sel_hi:[1,0,1]
	v_add_f32_e32 v11, v11, v15
	v_pk_fma_f32 v[20:21], v[20:21], v[72:73], v[22:23] op_sel_hi:[1,0,1]
	v_add_f32_e32 v22, v9, v13
	v_pk_fma_f32 v[20:21], v[52:53], v[86:87], v[20:21] op_sel_hi:[1,0,1]
	v_add_f32_e32 v23, v10, v14
	v_mov_b32_e32 v9, v54
	v_max_f32_e32 v10, 0, v7
	v_mov_b32_e32 v54, v17
	v_max_f32_e32 v14, 0, v22
	v_pk_fma_f32 v[8:9], v[8:9], v[10:11], v[20:21] op_sel_hi:[1,0,1]
	v_mov_b32_e32 v12, v18
	v_mov_b32_e32 v13, v56
	v_max_f32_e32 v16, 0, v23
	v_pk_fma_f32 v[8:9], v[54:55], v[14:15], v[8:9] op_sel_hi:[1,0,1]
	v_max_f32_e32 v22, 0, v11
	v_pk_fma_f32 v[8:9], v[12:13], v[16:17], v[8:9] op_sel_hi:[1,0,1]
	v_mov_b32_e32 v56, v19
	ds_read_b128 v[10:13], v32 offset:52432
	ds_read_b128 v[14:17], v32 offset:52688
	ds_read_b128 v[18:21], v32 offset:52944
	v_pk_fma_f32 v[22:23], v[56:57], v[22:23], v[8:9] op_sel_hi:[1,0,1]
	v_and_b32_e32 v24, 64, v84
	v_xor_b32_e32 v7, 16, v84
	v_add_u32_e32 v8, 64, v24
	v_cmp_lt_i32_e64 s[6:7], v7, v8
	s_and_b64 s[8:9], s[2:3], vcc
	s_waitcnt lgkmcnt(0)
	v_add_f32_e32 v9, v0, v10
	v_add_f32_e32 v11, v1, v11
	v_mov_b32_e32 v0, v14
	v_mov_b32_e32 v1, v18
	v_max_f32_e32 v10, 0, v9
	v_add_f32_e32 v24, v2, v12
	v_add_f32_e32 v13, v3, v13
	v_mov_b32_e32 v18, v15
	v_max_f32_e32 v12, 0, v11
	v_pk_fma_f32 v[0:1], v[0:1], v[10:11], v[22:23] op_sel_hi:[1,0,1]
	v_mov_b32_e32 v2, v16
	v_mov_b32_e32 v3, v20
	v_max_f32_e32 v14, 0, v24
	v_pk_fma_f32 v[0:1], v[18:19], v[12:13], v[0:1] op_sel_hi:[1,0,1]
	v_cndmask_b32_e64 v7, v84, v7, s[6:7]
	v_mov_b32_e32 v20, v17
	v_max_f32_e32 v16, 0, v13
	v_pk_fma_f32 v[0:1], v[2:3], v[14:15], v[0:1] op_sel_hi:[1,0,1]
	v_lshlrev_b32_e32 v7, 2, v7
	v_pk_fma_f32 v[0:1], v[20:21], v[16:17], v[0:1] op_sel_hi:[1,0,1]
	ds_bpermute_b32 v2, v7, v0
	ds_bpermute_b32 v3, v7, v1
	v_xor_b32_e32 v7, 32, v84
	v_cmp_lt_i32_e64 s[6:7], v7, v8
	v_mov_b32_e32 v10, -1
	s_waitcnt lgkmcnt(0)
	v_pk_add_f32 v[0:1], v[0:1], v[2:3]
	v_cndmask_b32_e64 v7, v84, v7, s[6:7]
	v_lshlrev_b32_e32 v7, 2, v7
	ds_bpermute_b32 v2, v7, v0
	ds_bpermute_b32 v3, v7, v1
	v_mov_b32_e32 v7, 0
	s_and_saveexec_b64 s[6:7], s[8:9]
	s_cbranch_execz .LBB5_108
	v_mov_b32_e32 v10, v115
	s_waitcnt lgkmcnt(0)
	v_pk_add_f32 v[4:5], v[0:1], v[2:3]
	v_mov_b32_e32 v7, 1.0
.LBB5_108:
	s_or_b64 exec, exec, s[6:7]
	v_lshlrev_b32_e32 v0, 2, v84
	v_and_b32_e32 v0, 0x100, v0
	ds_bpermute_b32 v9, v0, v10
	s_xor_b64 s[10:11], s[8:9], -1
	s_waitcnt lgkmcnt(0)
	v_cmp_eq_u32_e32 vcc, v10, v9
	s_or_b64 s[10:11], vcc, s[10:11]
	v_cndmask_b32_e64 v0, 0, 1, s[10:11]
	v_cmp_ne_u32_e32 vcc, 0, v0
	s_cmp_lg_u64 vcc, exec
	v_cmp_gt_i32_e64 s[6:7], 0, v9
	s_cselect_b64 s[10:11], -1, 0
	s_or_b64 s[10:11], s[6:7], s[10:11]
	s_mov_b64 s[6:7], 0
	s_and_saveexec_b64 s[34:35], s[10:11]
	s_xor_b64 s[10:11], exec, s[34:35]
	s_cbranch_execnz .LBB5_111
	s_or_saveexec_b64 s[8:9], s[10:11]
	v_mov_b32_e32 v10, 1.0
	s_xor_b64 exec, exec, s[8:9]
	s_cbranch_execnz .LBB5_114

	.amdhsa_kernel _Z7k_layerILi2EEvPKDF16_PKiPKjS3_S3_S1_PKfPDF16_PhS3_S7_Pf
		.amdhsa_group_segment_fixed_size 768
		.amdhsa_private_segment_fixed_size 0
		.amdhsa_kernarg_size 352
		.amdhsa_user_sgpr_count 2
		.amdhsa_user_sgpr_dispatch_ptr 0
		.amdhsa_user_sgpr_queue_ptr 0
		.amdhsa_user_sgpr_kernarg_segment_ptr 1
		.amdhsa_user_sgpr_dispatch_id 0
		.amdhsa_user_sgpr_kernarg_preload_length 0
		.amdhsa_user_sgpr_kernarg_preload_offset 0
		.amdhsa_user_sgpr_private_segment_size 0
		.amdhsa_uses_dynamic_stack 0
		.amdhsa_enable_private_segment 0
		.amdhsa_system_sgpr_workgroup_id_x 1
		.amdhsa_system_sgpr_workgroup_id_y 0
		.amdhsa_system_sgpr_workgroup_id_z 0
		.amdhsa_system_sgpr_workgroup_info 0
		.amdhsa_system_vgpr_workitem_id 0
		.amdhsa_next_free_vgpr 118
		.amdhsa_next_free_sgpr 43
		.amdhsa_accum_offset 120
		.amdhsa_reserve_vcc 1
		.amdhsa_float_round_mode_32 0
		.amdhsa_float_round_mode_16_64 0
		.amdhsa_float_denorm_mode_32 3
		.amdhsa_float_denorm_mode_16_64 3
		.amdhsa_dx10_clamp 1
		.amdhsa_ieee_mode 1
		.amdhsa_fp16_overflow 0
		.amdhsa_tg_split 0
		.amdhsa_exception_fp_ieee_invalid_op 0
		.amdhsa_exception_fp_denorm_src 0
		.amdhsa_exception_fp_ieee_div_zero 0
		.amdhsa_exception_fp_ieee_overflow 0
		.amdhsa_exception_fp_ieee_underflow 0
		.amdhsa_exception_fp_ieee_inexact 0
		.amdhsa_exception_int_div_zero 0
	.end_amdhsa_kernel

amdhsa.kernels:
  - .agpr_count:     0
    .args:
      - .actual_access:  read_only
        .address_space:  global
        .offset:         0
        .size:           8
        .value_kind:     global_buffer
      - .actual_access:  read_only
        .address_space:  global
        .offset:         8
        .size:           8
        .value_kind:     global_buffer
      - .actual_access:  read_only
        .address_space:  global
        .offset:         16
        .size:           8
        .value_kind:     global_buffer
      - .actual_access:  read_only
        .address_space:  global
        .offset:         24
        .size:           8
        .value_kind:     global_buffer
      - .actual_access:  read_only
        .address_space:  global
        .offset:         32
        .size:           8
        .value_kind:     global_buffer
      - .actual_access:  read_only
        .address_space:  global
        .offset:         40
        .size:           8
        .value_kind:     global_buffer
      - .actual_access:  read_only
        .address_space:  global
        .offset:         48
        .size:           8
        .value_kind:     global_buffer
      - .actual_access:  read_only
        .address_space:  global
        .offset:         56
        .size:           8
        .value_kind:     global_buffer
      - .actual_access:  read_only
        .address_space:  global
        .offset:         64
        .size:           8
        .value_kind:     global_buffer
      - .actual_access:  read_only
        .address_space:  global
        .offset:         72
        .size:           8
        .value_kind:     global_buffer
      - .actual_access:  read_only
        .address_space:  global
        .offset:         80
        .size:           8
        .value_kind:     global_buffer
      - .actual_access:  read_only
        .address_space:  global
        .offset:         88
        .size:           8
        .value_kind:     global_buffer
      - .actual_access:  write_only
        .address_space:  global
        .offset:         96
        .size:           8
        .value_kind:     global_buffer
      - .actual_access:  write_only
        .address_space:  global
        .offset:         104
        .size:           8
        .value_kind:     global_buffer
      - .actual_access:  write_only
        .address_space:  global
        .offset:         112
        .size:           8
        .value_kind:     global_buffer
      - .actual_access:  write_only
        .address_space:  global
        .offset:         120
        .size:           8
        .value_kind:     global_buffer
      - .actual_access:  write_only
        .address_space:  global
        .offset:         128
        .size:           8
        .value_kind:     global_buffer
      - .actual_access:  write_only
        .address_space:  global
        .offset:         136
        .size:           8
        .value_kind:     global_buffer
      - .actual_access:  write_only
        .address_space:  global
        .offset:         144
        .size:           8
        .value_kind:     global_buffer
      - .actual_access:  write_only
        .address_space:  global
        .offset:         152
        .size:           8
        .value_kind:     global_buffer
      - .actual_access:  write_only
        .address_space:  global
        .offset:         160
        .size:           8
        .value_kind:     global_buffer
    .group_segment_fixed_size: 0
    .kernarg_segment_align: 8
    .kernarg_segment_size: 168
    .language:       OpenCL C
    .language_version:
      - 2
      - 0
    .max_flat_workgroup_size: 1024
    .name:           _Z6k_prepPKiS0_PKfS2_S2_S2_S2_S2_S2_S2_S2_S2_PDF16_S3_S3_PfS4_S4_PjS3_S5_
    .private_segment_fixed_size: 0
    .sgpr_count:     27
    .sgpr_spill_count: 0
    .symbol:         _Z6k_prepPKiS0_PKfS2_S2_S2_S2_S2_S2_S2_S2_S2_PDF16_S3_S3_PfS4_S4_PjS3_S5_.kd
    .uniform_work_group_size: 1
    .uses_dynamic_stack: false
    .vgpr_count:     61
    .vgpr_spill_count: 0
    .wavefront_size: 64
  - .agpr_count:     0
    .args:
      - .actual_access:  read_only
        .address_space:  global
        .offset:         0
        .size:           8
        .value_kind:     global_buffer
      - .actual_access:  read_only
        .address_space:  global
        .offset:         8
        .size:           8
        .value_kind:     global_buffer
      - .actual_access:  read_only
        .address_space:  global
        .offset:         16
        .size:           8
        .value_kind:     global_buffer
      - .actual_access:  write_only
        .address_space:  global
        .offset:         24
        .size:           8
        .value_kind:     global_buffer
      - .actual_access:  write_only
        .address_space:  global
        .offset:         32
        .size:           8
        .value_kind:     global_buffer
      - .actual_access:  write_only
        .address_space:  global
        .offset:         40
        .size:           8
        .value_kind:     global_buffer
      - .actual_access:  read_only
        .address_space:  global
        .offset:         48
        .size:           8
        .value_kind:     global_buffer
      - .actual_access:  read_only
        .address_space:  global
        .offset:         56
        .size:           8
        .value_kind:     global_buffer
      - .actual_access:  read_only
        .address_space:  global
        .offset:         64
        .size:           8
        .value_kind:     global_buffer
      - .actual_access:  read_only
        .address_space:  global
        .offset:         72
        .size:           8
        .value_kind:     global_buffer
      - .actual_access:  read_only
        .address_space:  global
        .offset:         80
        .size:           8
        .value_kind:     global_buffer
      - .actual_access:  read_only
        .address_space:  global
        .offset:         88
        .size:           8
        .value_kind:     global_buffer
      - .actual_access:  read_only
        .address_space:  global
        .offset:         96
        .size:           8
        .value_kind:     global_buffer
      - .actual_access:  read_only
        .address_space:  global
        .offset:         104
        .size:           8
        .value_kind:     global_buffer
      - .actual_access:  read_only
        .address_space:  global
        .offset:         112
        .size:           8
        .value_kind:     global_buffer
      - .actual_access:  read_only
        .address_space:  global
        .offset:         120
        .size:           8
        .value_kind:     global_buffer
      - .actual_access:  read_only
        .address_space:  global
        .offset:         128
        .size:           8
        .value_kind:     global_buffer
      - .actual_access:  write_only
        .address_space:  global
        .offset:         136
        .size:           8
        .value_kind:     global_buffer
      - .actual_access:  write_only
        .address_space:  global
        .offset:         144
        .size:           8
        .value_kind:     global_buffer
      - .actual_access:  write_only
        .address_space:  global
        .offset:         152
        .size:           8
        .value_kind:     global_buffer
      - .actual_access:  write_only
        .address_space:  global
        .offset:         160
        .size:           8
        .value_kind:     global_buffer
      - .actual_access:  write_only
        .address_space:  global
        .offset:         168
        .size:           8
        .value_kind:     global_buffer
    .group_segment_fixed_size: 1696
    .kernarg_segment_align: 8
    .kernarg_segment_size: 176
    .language:       OpenCL C
    .language_version:
      - 2
      - 0
    .max_flat_workgroup_size: 1024
    .name:           _Z11k_localsortPKiS0_S0_PjPtPiPKjPKfS7_S7_S7_S7_S7_S7_S7_S7_S7_PDF16_S8_S8_PfS9_
    .private_segment_fixed_size: 0
    .sgpr_count:     71
    .sgpr_spill_count: 0
    .symbol:         _Z11k_localsortPKiS0_S0_PjPtPiPKjPKfS7_S7_S7_S7_S7_S7_S7_S7_S7_PDF16_S8_S8_PfS9_.kd
    .uniform_work_group_size: 1
    .uses_dynamic_stack: false
    .vgpr_count:     95
    .vgpr_spill_count: 0
    .wavefront_size: 64
  - .agpr_count:     0
    .args:
      - .actual_access:  read_only
        .address_space:  global
        .offset:         0
        .size:           8
        .value_kind:     global_buffer
      - .actual_access:  read_only
        .address_space:  global
        .offset:         8
        .size:           8
        .value_kind:     global_buffer
      - .actual_access:  read_only
        .address_space:  global
        .offset:         16
        .size:           8
        .value_kind:     global_buffer
      - .actual_access:  write_only
        .address_space:  global
        .offset:         24
        .size:           8
        .value_kind:     global_buffer
      - .actual_access:  write_only
        .address_space:  global
        .offset:         32
        .size:           8
        .value_kind:     global_buffer
    .group_segment_fixed_size: 54144
    .kernarg_segment_align: 8
    .kernarg_segment_size: 40
    .language:       OpenCL C
    .language_version:
      - 2
      - 0
    .max_flat_workgroup_size: 1024
    .name:           _Z12k_bucketsortPKjPKtPKiPiPj
    .private_segment_fixed_size: 0
    .sgpr_count:     70
    .sgpr_spill_count: 0
    .symbol:         _Z12k_bucketsortPKjPKtPKiPiPj.kd
    .uniform_work_group_size: 1
    .uses_dynamic_stack: false
    .vgpr_count:     64
    .vgpr_spill_count: 0
    .wavefront_size: 64
  - .agpr_count:     0
    .args:
      - .actual_access:  read_only
        .address_space:  global
        .offset:         0
        .size:           8
        .value_kind:     global_buffer
      - .actual_access:  read_only
        .address_space:  global
        .offset:         8
        .size:           8
        .value_kind:     global_buffer
      - .actual_access:  write_only
        .address_space:  global
        .offset:         16
        .size:           8
        .value_kind:     global_buffer
    .group_segment_fixed_size: 0
    .kernarg_segment_align: 8
    .kernarg_segment_size: 24
    .language:       OpenCL C
    .language_version:
      - 2
      - 0
    .max_flat_workgroup_size: 256
    .name:           _Z7k_finalPKfS0_Pf
    .private_segment_fixed_size: 0
    .sgpr_count:     14
    .sgpr_spill_count: 0
    .symbol:         _Z7k_finalPKfS0_Pf.kd
    .uniform_work_group_size: 1
    .uses_dynamic_stack: false
    .vgpr_count:     10
    .vgpr_spill_count: 0
    .wavefront_size: 64
  - .agpr_count:     0
    .args:
      - .actual_access:  read_only
        .address_space:  global
        .offset:         0
        .size:           8
        .value_kind:     global_buffer
      - .actual_access:  read_only
        .address_space:  global
        .offset:         8
        .size:           8
        .value_kind:     global_buffer
      - .actual_access:  read_only
        .address_space:  global
        .offset:         16
        .size:           8
        .value_kind:     global_buffer
      - .actual_access:  read_only
        .address_space:  global
        .offset:         24
        .size:           8
        .value_kind:     global_buffer
      - .actual_access:  read_only
        .address_space:  global
        .offset:         32
        .size:           8
        .value_kind:     global_buffer
      - .actual_access:  read_only
        .address_space:  global
        .offset:         40
        .size:           8
        .value_kind:     global_buffer
      - .address_space:  global
        .offset:         48
        .size:           8
        .value_kind:     global_buffer
      - .actual_access:  write_only
        .address_space:  global
        .offset:         56
        .size:           8
        .value_kind:     global_buffer
      - .address_space:  global
        .offset:         64
        .size:           8
        .value_kind:     global_buffer
      - .actual_access:  read_only
        .address_space:  global
        .offset:         72
        .size:           8
        .value_kind:     global_buffer
      - .address_space:  global
        .offset:         80
        .size:           8
        .value_kind:     global_buffer
      - .actual_access:  read_only
        .address_space:  global
        .offset:         88
        .size:           8
        .value_kind:     global_buffer
      - .offset:         96
        .size:           4
        .value_kind:     hidden_block_count_x
      - .offset:         100
        .size:           4
        .value_kind:     hidden_block_count_y
      - .offset:         104
        .size:           4
        .value_kind:     hidden_block_count_z
      - .offset:         108
        .size:           2
        .value_kind:     hidden_group_size_x
      - .offset:         110
        .size:           2
        .value_kind:     hidden_group_size_y
      - .offset:         112
        .size:           2
        .value_kind:     hidden_group_size_z
      - .offset:         114
        .size:           2
        .value_kind:     hidden_remainder_x
      - .offset:         116
        .size:           2
        .value_kind:     hidden_remainder_y
      - .offset:         118
        .size:           2
        .value_kind:     hidden_remainder_z
      - .offset:         136
        .size:           8
        .value_kind:     hidden_global_offset_x
      - .offset:         144
        .size:           8
        .value_kind:     hidden_global_offset_y
      - .offset:         152
        .size:           8
        .value_kind:     hidden_global_offset_z
      - .offset:         160
        .size:           2
        .value_kind:     hidden_grid_dims
      - .offset:         216
        .size:           4
        .value_kind:     hidden_dynamic_lds_size
    .group_segment_fixed_size: 256
    .kernarg_segment_align: 8
    .kernarg_segment_size: 352
    .language:       OpenCL C
    .language_version:
      - 2
      - 0
    .max_flat_workgroup_size: 1024
    .name:           _Z7k_layerILi1EEvPKDF16_PKiPKjS3_S3_S1_PKfPDF16_PhS3_S7_Pf
    .private_segment_fixed_size: 0
    .sgpr_count:     38
    .sgpr_spill_count: 0
    .symbol:         _Z7k_layerILi1EEvPKDF16_PKiPKjS3_S3_S1_PKfPDF16_PhS3_S7_Pf.kd
    .uniform_work_group_size: 1
    .uses_dynamic_stack: false
    .vgpr_count:     114
    .vgpr_spill_count: 0
    .wavefront_size: 64
  - .agpr_count:     0
    .args:
      - .actual_access:  read_only
        .address_space:  global
        .offset:         0
        .size:           8
        .value_kind:     global_buffer
      - .actual_access:  read_only
        .address_space:  global
        .offset:         8
        .size:           8
        .value_kind:     global_buffer
      - .actual_access:  read_only
        .address_space:  global
        .offset:         16
        .size:           8
        .value_kind:     global_buffer
      - .actual_access:  read_only
        .address_space:  global
        .offset:         24
        .size:           8
        .value_kind:     global_buffer
      - .actual_access:  read_only
        .address_space:  global
        .offset:         32
        .size:           8
        .value_kind:     global_buffer
      - .actual_access:  read_only
        .address_space:  global
        .offset:         40
        .size:           8
        .value_kind:     global_buffer
      - .address_space:  global
        .offset:         48
        .size:           8
        .value_kind:     global_buffer
      - .actual_access:  read_only
        .address_space:  global
        .offset:         56
        .size:           8
        .value_kind:     global_buffer
      - .address_space:  global
        .offset:         64
        .size:           8
        .value_kind:     global_buffer
      - .actual_access:  read_only
        .address_space:  global
        .offset:         72
        .size:           8
        .value_kind:     global_buffer
      - .address_space:  global
        .offset:         80
        .size:           8
        .value_kind:     global_buffer
      - .address_space:  global
        .offset:         88
        .size:           8
        .value_kind:     global_buffer
      - .offset:         96
        .size:           4
        .value_kind:     hidden_block_count_x
      - .offset:         100
        .size:           4
        .value_kind:     hidden_block_count_y
      - .offset:         104
        .size:           4
        .value_kind:     hidden_block_count_z
      - .offset:         108
        .size:           2
        .value_kind:     hidden_group_size_x
      - .offset:         110
        .size:           2
        .value_kind:     hidden_group_size_y
      - .offset:         112
        .size:           2
        .value_kind:     hidden_group_size_z
      - .offset:         114
        .size:           2
        .value_kind:     hidden_remainder_x
      - .offset:         116
        .size:           2
        .value_kind:     hidden_remainder_y
      - .offset:         118
        .size:           2
        .value_kind:     hidden_remainder_z
      - .offset:         136
        .size:           8
        .value_kind:     hidden_global_offset_x
      - .offset:         144
        .size:           8
        .value_kind:     hidden_global_offset_y
      - .offset:         152
        .size:           8
        .value_kind:     hidden_global_offset_z
      - .offset:         160
        .size:           2
        .value_kind:     hidden_grid_dims
      - .offset:         216
        .size:           4
        .value_kind:     hidden_dynamic_lds_size
    .group_segment_fixed_size: 768
    .kernarg_segment_align: 8
    .kernarg_segment_size: 352
    .language:       OpenCL C
    .language_version:
      - 2
      - 0
    .max_flat_workgroup_size: 1024
    .name:           _Z7k_layerILi2EEvPKDF16_PKiPKjS3_S3_S1_PKfPDF16_PhS3_S7_Pf
    .private_segment_fixed_size: 0
    .sgpr_count:     49
    .sgpr_spill_count: 0
    .symbol:         _Z7k_layerILi2EEvPKDF16_PKiPKjS3_S3_S1_PKfPDF16_PhS3_S7_Pf.kd
    .uniform_work_group_size: 1
    .uses_dynamic_stack: false
    .vgpr_count:     118
    .vgpr_spill_count: 0
    .wavefront_size: 64
